# v77 + per-workgroup code histogram through LDS atomics
# speedup vs baseline: 1.0143x; 1.0143x over previous
_Z7vq_mainPKfPKiS0_PfPhPdPi:
	s_load_dwordx4 s[4:7], s[0:1], 0x0
	s_load_dwordx2 s[22:23], s[0:1], 0x10
	s_load_dwordx2 s[20:21], s[0:1], 0x18
	s_load_dwordx4 s[12:15], s[0:1], 0x20
	s_load_dwordx2 s[10:11], s[0:1], 0x30
	s_and_b32 s3, s2, 7
	s_lshl_b32 s3, s3, 6
	s_lshr_b32 s16, s2, 3
	s_add_i32 s16, s16, s3
	s_lshr_b32 s18, s16, 5
	s_mov_b32 s19, 0
	s_and_b32 s28, s16, 31
	s_lshl_b32 s28, s28, 4
	s_add_i32 s29, s28, 1
	v_readfirstlane_b32 s17, v0
	v_and_b32_e32 v1, 63, v0
	v_lshlrev_b32_e32 v66, 4, v0
	s_lshr_b32 s17, s17, 6
	s_lshl_b32 s24, s17, 4
	s_lshl_b32 s30, s18, 15
	s_lshl_b32 s31, s18, 23
	v_add_u32_e32 v67, 0x1000, v66
	v_add_u32_e32 v68, 0x2000, v66
	v_add_u32_e32 v69, 0x3000, v66
	v_add_u32_e32 v70, 0x4000, v66
	v_add_u32_e32 v71, 0x5000, v66
	v_add_u32_e32 v72, 0x6000, v66
	v_add_u32_e32 v73, 0x7000, v66
	s_movk_i32 s9, 0x810
	s_mov_b32 s3, 0x8100
	s_mul_i32 s36, s29, 0x810
	v_mov_b32_e32 v141, s36
	v_sub_u32_e32 v141, 0, v141
	s_waitcnt lgkmcnt(0)
	s_add_u32 s34, s6, s30
	s_addc_u32 s35, s7, 0
	s_add_u32 s32, s4, s31
	s_addc_u32 s33, s5, 0
	global_load_dwordx4 v[74:77], v66, s[34:35]
	global_load_dwordx4 v[78:81], v67, s[34:35]
	global_load_dwordx4 v[82:85], v68, s[34:35]
	global_load_dwordx4 v[86:89], v69, s[34:35]
	global_load_dwordx4 v[90:93], v70, s[34:35]
	global_load_dwordx4 v[94:97], v71, s[34:35]
	global_load_dwordx4 v[98:101], v72, s[34:35]
	global_load_dwordx4 v[102:105], v73, s[34:35]
	v_and_b32_e32 v150, 15, v0
	v_or_b32_e32 v150, s24, v150
	v_and_b32_e32 v151, 48, v0
	v_lshl_or_b32 v150, v150, 10, v151
	global_load_dwordx4 v[62:65], v150, s[22:23] offset:0
	global_load_dwordx4 v[58:61], v150, s[22:23] offset:64
	global_load_dwordx4 v[54:57], v150, s[22:23] offset:128
	global_load_dwordx4 v[50:53], v150, s[22:23] offset:192
	global_load_dwordx4 v[46:49], v150, s[22:23] offset:256
	global_load_dwordx4 v[42:45], v150, s[22:23] offset:320
	global_load_dwordx4 v[38:41], v150, s[22:23] offset:384
	global_load_dwordx4 v[34:37], v150, s[22:23] offset:448
	global_load_dwordx4 v[30:33], v150, s[22:23] offset:512
	global_load_dwordx4 v[26:29], v150, s[22:23] offset:576
	global_load_dwordx4 v[22:25], v150, s[22:23] offset:640
	global_load_dwordx4 v[18:21], v150, s[22:23] offset:704
	global_load_dwordx4 v[14:17], v150, s[22:23] offset:768
	global_load_dwordx4 v[10:13], v150, s[22:23] offset:832
	global_load_dwordx4 v[6:9], v150, s[22:23] offset:896
	global_load_dwordx4 v[2:5], v150, s[22:23] offset:960
	v_and_b32_e32 v138, 15, v0
	v_lshlrev_b32_e32 v139, 2, v1
	v_bfe_u32 v140, v0, 4, 2
	v_mov_b32_e32 v142, 1
	v_mov_b32_e32 v143, 4
	v_mov_b32_e32 v144, 0x11100
	v_lshlrev_b32_e32 v145, 8, v0
	v_lshlrev_b32_e32 v148, 3, v0
	v_mov_b32_e32 v152, 0
	v_mov_b32_e32 v153, 0
	ds_write_b64 v148, v[152:153] offset:32768
	ds_write_b64 v148, v[152:153] offset:34832
	ds_write_b64 v148, v[152:153] offset:36896
	ds_write_b64 v148, v[152:153] offset:38960
	ds_write_b64 v148, v[152:153] offset:41024
	ds_write_b64 v148, v[152:153] offset:43088
	ds_write_b64 v148, v[152:153] offset:45152
	ds_write_b64 v148, v[152:153] offset:47216
	ds_write_b64 v148, v[152:153] offset:49280
	ds_write_b64 v148, v[152:153] offset:51344
	ds_write_b64 v148, v[152:153] offset:53408
	ds_write_b64 v148, v[152:153] offset:55472
	ds_write_b64 v148, v[152:153] offset:57536
	ds_write_b64 v148, v[152:153] offset:59600
	ds_write_b64 v148, v[152:153] offset:61664
	ds_write_b64 v148, v[152:153] offset:63728
	v_cmp_gt_u32_e32 vcc, 16, v0
	s_and_saveexec_b64 s[30:31], vcc
	v_mul_u32_u24_e32 v151, 0x810, v0
	ds_write_b64 v151, v[152:153] offset:34816
	v_mov_b32_e32 v150, 0x11540
	v_mov_b32_e32 v149, 8
	ds_write_b32 v150, v149
	s_mov_b64 exec, s[30:31]
	v_cmp_gt_u32_e32 vcc, 64, v0
	s_and_saveexec_b64 s[30:31], vcc
	v_mov_b32_e32 v150, 0x11600
	v_lshl_add_u32 v150, v0, 2, v150
	ds_write_b32 v150, v152
	s_mov_b64 exec, s[30:31]
	s_waitcnt lgkmcnt(0)
	s_barrier
	s_waitcnt vmcnt(16)
	v_mad_u32_u24 v74, v74, s9, v141
	v_mad_u32_u24 v75, v75, s9, v141
	v_mad_u32_u24 v76, v76, s9, v141
	v_mad_u32_u24 v77, v77, s9, v141
	v_mad_u32_u24 v78, v78, s9, v141
	v_mad_u32_u24 v79, v79, s9, v141
	v_mad_u32_u24 v80, v80, s9, v141
	v_mad_u32_u24 v81, v81, s9, v141
	v_mad_u32_u24 v82, v82, s9, v141
	v_mad_u32_u24 v83, v83, s9, v141
	v_mad_u32_u24 v84, v84, s9, v141
	v_mad_u32_u24 v85, v85, s9, v141
	v_mad_u32_u24 v86, v86, s9, v141
	v_mad_u32_u24 v87, v87, s9, v141
	v_mad_u32_u24 v88, v88, s9, v141
	v_mad_u32_u24 v89, v89, s9, v141
	v_mad_u32_u24 v90, v90, s9, v141
	v_mad_u32_u24 v91, v91, s9, v141
	v_mad_u32_u24 v92, v92, s9, v141
	v_mad_u32_u24 v93, v93, s9, v141
	v_mad_u32_u24 v94, v94, s9, v141
	v_mad_u32_u24 v95, v95, s9, v141
	v_mad_u32_u24 v96, v96, s9, v141
	v_mad_u32_u24 v97, v97, s9, v141
	v_mad_u32_u24 v98, v98, s9, v141
	v_mad_u32_u24 v99, v99, s9, v141
	v_mad_u32_u24 v100, v100, s9, v141
	v_mad_u32_u24 v101, v101, s9, v141
	v_mad_u32_u24 v102, v102, s9, v141
	v_mad_u32_u24 v103, v103, s9, v141
	v_mad_u32_u24 v104, v104, s9, v141
	v_mad_u32_u24 v105, v105, s9, v141
	v_cmp_gt_u32_e64 s[36:37], s3, v74
	v_cmp_gt_u32_e64 s[38:39], s3, v75
	v_cmp_gt_u32_e64 s[40:41], s3, v76
	v_cmp_gt_u32_e64 s[42:43], s3, v77
	v_cmp_gt_u32_e64 s[44:45], s3, v78
	v_cmp_gt_u32_e64 s[46:47], s3, v79
	v_cmp_gt_u32_e64 s[48:49], s3, v80
	v_cmp_gt_u32_e64 s[50:51], s3, v81
	v_cmp_gt_u32_e64 s[52:53], s3, v82
	v_cmp_gt_u32_e64 s[54:55], s3, v83
	v_cmp_gt_u32_e64 s[56:57], s3, v84
	v_cmp_gt_u32_e64 s[58:59], s3, v85
	v_cmp_gt_u32_e64 s[60:61], s3, v86
	v_cmp_gt_u32_e64 s[62:63], s3, v87
	v_cmp_gt_u32_e64 s[64:65], s3, v88
	v_cmp_gt_u32_e64 s[66:67], s3, v89
	v_cmp_gt_u32_e64 s[68:69], s3, v90
	v_cmp_gt_u32_e64 s[70:71], s3, v91
	v_cmp_gt_u32_e64 s[72:73], s3, v92
	v_cmp_gt_u32_e64 s[74:75], s3, v93
	v_cmp_gt_u32_e64 s[76:77], s3, v94
	v_cmp_gt_u32_e64 s[78:79], s3, v95
	v_cmp_gt_u32_e64 s[80:81], s3, v96
	v_cmp_gt_u32_e64 s[82:83], s3, v97
	v_cmp_gt_u32_e64 s[84:85], s3, v98
	v_cmp_gt_u32_e64 s[86:87], s3, v99
	v_cmp_gt_u32_e64 s[88:89], s3, v100
	v_cmp_gt_u32_e64 s[90:91], s3, v101
	v_cmp_gt_u32_e64 s[92:93], s3, v102
	v_cmp_gt_u32_e64 s[94:95], s3, v103
	v_cmp_gt_u32_e64 s[96:97], s3, v104
	v_cmp_gt_u32_e64 s[98:99], s3, v105
	s_mov_b64 exec, s[36:37]
	ds_add_u32 v74, v142 offset:34816
	s_mov_b64 exec, s[38:39]
	ds_add_u32 v75, v142 offset:34816
	s_mov_b64 exec, s[40:41]
	ds_add_u32 v76, v142 offset:34816
	s_mov_b64 exec, s[42:43]
	ds_add_u32 v77, v142 offset:34816
	s_mov_b64 exec, s[44:45]
	ds_add_u32 v78, v142 offset:34816
	s_mov_b64 exec, s[46:47]
	ds_add_u32 v79, v142 offset:34816
	s_mov_b64 exec, s[48:49]
	ds_add_u32 v80, v142 offset:34816
	s_mov_b64 exec, s[50:51]
	ds_add_u32 v81, v142 offset:34816
	s_mov_b64 exec, s[52:53]
	ds_add_u32 v82, v142 offset:34816
	s_mov_b64 exec, s[54:55]
	ds_add_u32 v83, v142 offset:34816
	s_mov_b64 exec, s[56:57]
	ds_add_u32 v84, v142 offset:34816
	s_mov_b64 exec, s[58:59]
	ds_add_u32 v85, v142 offset:34816
	s_mov_b64 exec, s[60:61]
	ds_add_u32 v86, v142 offset:34816
	s_mov_b64 exec, s[62:63]
	ds_add_u32 v87, v142 offset:34816
	s_mov_b64 exec, s[64:65]
	ds_add_u32 v88, v142 offset:34816
	s_mov_b64 exec, s[66:67]
	ds_add_u32 v89, v142 offset:34816
	s_mov_b64 exec, s[68:69]
	ds_add_u32 v90, v142 offset:34816
	s_mov_b64 exec, s[70:71]
	ds_add_u32 v91, v142 offset:34816
	s_mov_b64 exec, s[72:73]
	ds_add_u32 v92, v142 offset:34816
	s_mov_b64 exec, s[74:75]
	ds_add_u32 v93, v142 offset:34816
	s_mov_b64 exec, s[76:77]
	ds_add_u32 v94, v142 offset:34816
	s_mov_b64 exec, s[78:79]
	ds_add_u32 v95, v142 offset:34816
	s_mov_b64 exec, s[80:81]
	ds_add_u32 v96, v142 offset:34816
	s_mov_b64 exec, s[82:83]
	ds_add_u32 v97, v142 offset:34816
	s_mov_b64 exec, s[84:85]
	ds_add_u32 v98, v142 offset:34816
	s_mov_b64 exec, s[86:87]
	ds_add_u32 v99, v142 offset:34816
	s_mov_b64 exec, s[88:89]
	ds_add_u32 v100, v142 offset:34816
	s_mov_b64 exec, s[90:91]
	ds_add_u32 v101, v142 offset:34816
	s_mov_b64 exec, s[92:93]
	ds_add_u32 v102, v142 offset:34816
	s_mov_b64 exec, s[94:95]
	ds_add_u32 v103, v142 offset:34816
	s_mov_b64 exec, s[96:97]
	ds_add_u32 v104, v142 offset:34816
	s_mov_b64 exec, s[98:99]
	ds_add_u32 v105, v142 offset:34816
	s_mov_b64 exec, -1
	s_waitcnt lgkmcnt(0)
	s_barrier
	s_waitcnt vmcnt(0)
	v_mul_f32_e32 v150, v62, v62
	v_mul_f32_e32 v151, v63, v63
	v_mul_f32_e32 v152, v64, v64
	v_mul_f32_e32 v153, v65, v65
	v_fmac_f32_e32 v150, v58, v58
	v_fmac_f32_e32 v151, v59, v59
	v_fmac_f32_e32 v152, v60, v60
	v_fmac_f32_e32 v153, v61, v61
	v_fmac_f32_e32 v150, v54, v54
	v_fmac_f32_e32 v151, v55, v55
	v_fmac_f32_e32 v152, v56, v56
	v_fmac_f32_e32 v153, v57, v57
	v_fmac_f32_e32 v150, v50, v50
	v_fmac_f32_e32 v151, v51, v51
	v_fmac_f32_e32 v152, v52, v52
	v_fmac_f32_e32 v153, v53, v53
	v_fmac_f32_e32 v150, v46, v46
	v_fmac_f32_e32 v151, v47, v47
	v_fmac_f32_e32 v152, v48, v48
	v_fmac_f32_e32 v153, v49, v49
	v_fmac_f32_e32 v150, v42, v42
	v_fmac_f32_e32 v151, v43, v43
	v_fmac_f32_e32 v152, v44, v44
	v_fmac_f32_e32 v153, v45, v45
	v_fmac_f32_e32 v150, v38, v38
	v_fmac_f32_e32 v151, v39, v39
	v_fmac_f32_e32 v152, v40, v40
	v_fmac_f32_e32 v153, v41, v41
	v_fmac_f32_e32 v150, v34, v34
	v_fmac_f32_e32 v151, v35, v35
	v_fmac_f32_e32 v152, v36, v36
	v_fmac_f32_e32 v153, v37, v37
	v_fmac_f32_e32 v150, v30, v30
	v_fmac_f32_e32 v151, v31, v31
	v_fmac_f32_e32 v152, v32, v32
	v_fmac_f32_e32 v153, v33, v33
	v_fmac_f32_e32 v150, v26, v26
	v_fmac_f32_e32 v151, v27, v27
	v_fmac_f32_e32 v152, v28, v28
	v_fmac_f32_e32 v153, v29, v29
	v_fmac_f32_e32 v150, v22, v22
	v_fmac_f32_e32 v151, v23, v23
	v_fmac_f32_e32 v152, v24, v24
	v_fmac_f32_e32 v153, v25, v25
	v_fmac_f32_e32 v150, v18, v18
	v_fmac_f32_e32 v151, v19, v19
	v_fmac_f32_e32 v152, v20, v20
	v_fmac_f32_e32 v153, v21, v21
	v_fmac_f32_e32 v150, v14, v14
	v_fmac_f32_e32 v151, v15, v15
	v_fmac_f32_e32 v152, v16, v16
	v_fmac_f32_e32 v153, v17, v17
	v_fmac_f32_e32 v150, v10, v10
	v_fmac_f32_e32 v151, v11, v11
	v_fmac_f32_e32 v152, v12, v12
	v_fmac_f32_e32 v153, v13, v13
	v_fmac_f32_e32 v150, v6, v6
	v_fmac_f32_e32 v151, v7, v7
	v_fmac_f32_e32 v152, v8, v8
	v_fmac_f32_e32 v153, v9, v9
	v_fmac_f32_e32 v150, v2, v2
	v_fmac_f32_e32 v151, v3, v3
	v_fmac_f32_e32 v152, v4, v4
	v_fmac_f32_e32 v153, v5, v5
	v_add_f32_e32 v150, v150, v151
	v_add_f32_e32 v152, v152, v153
	v_add_f32_e32 v150, v150, v152
	v_mbcnt_lo_u32_b32 v151, -1, 0
	v_mbcnt_hi_u32_b32 v151, -1, v151
	v_xor_b32_e32 v152, 16, v151
	v_lshlrev_b32_e32 v152, 2, v152
	ds_bpermute_b32 v152, v152, v150
	v_xor_b32_e32 v153, 32, v151
	v_lshlrev_b32_e32 v153, 2, v153
	s_waitcnt lgkmcnt(0)
	v_add_f32_e32 v150, v150, v152
	ds_bpermute_b32 v153, v153, v150
	v_add_u32_e32 v152, s24, v1
	v_lshlrev_b32_e32 v152, 2, v152
	v_add_u32_e32 v152, 0x11300, v152
	v_cmp_gt_u32_e32 vcc, 16, v1
	s_and_saveexec_b64 s[30:31], vcc
	s_waitcnt lgkmcnt(0)
	v_add_f32_e32 v150, v150, v153
	ds_write_b32 v152, v150
	s_mov_b64 exec, s[30:31]
	v_and_b32_e32 v67, 15, v0
	v_mul_u32_u24_e32 v67, 0x810, v67
	ds_read_b32 v68, v67 offset:34816
	s_waitcnt lgkmcnt(0)
	v_mov_b32_e32 v69, v68
	s_nop 1
	v_add_u32_dpp v69, v69, v69 row_shr:1 row_mask:0xf bank_mask:0xf bound_ctrl:1
	s_nop 1
	v_add_u32_dpp v69, v69, v69 row_shr:2 row_mask:0xf bank_mask:0xf bound_ctrl:1
	s_nop 1
	v_add_u32_dpp v69, v69, v69 row_shr:4 row_mask:0xf bank_mask:0xf bound_ctrl:1
	s_nop 1
	v_add_u32_dpp v69, v69, v69 row_shr:8 row_mask:0xf bank_mask:0xf bound_ctrl:1
	s_nop 1
	v_sub_u32_e32 v70, v69, v68
	v_lshlrev_b32_e32 v70, 2, v70
	v_readlane_b32 s8, v69, 15
	s_cmp_lg_u32 s17, 0
	s_cbranch_scc1 .Lfront_nocursor
	v_cmp_gt_u32_e32 vcc, 16, v1
	s_and_saveexec_b64 s[30:31], vcc
	ds_write_b32 v67, v70 offset:34820
	v_lshl_add_u32 v71, v1, 2, v144
	ds_write_b32 v71, v68
	v_max_i32_e32 v150, 1, v68
	v_cvt_f32_u32_e32 v150, v150
	v_div_scale_f32 v151, s[100:101], v150, v150, 1.0
	v_rcp_f32_e32 v152, v151
	v_div_scale_f32 v153, vcc, 1.0, v150, 1.0
	v_fma_f32 v154, -v151, v152, 1.0
	v_fmac_f32_e32 v152, v154, v152
	v_mul_f32_e32 v154, v153, v152
	v_fma_f32 v155, -v151, v154, v153
	v_fmac_f32_e32 v154, v155, v152
	v_fma_f32 v153, -v151, v154, v153
	v_div_fmas_f32 v155, v153, v152, v154
	v_div_fixup_f32 v156, v155, v150, 1.0
	ds_write_b32 v71, v156 offset:320
	s_mov_b64 exec, s[30:31]

.Lg_alldone:
.Lg_nocopy:
	v_mov_b32_e32 v97, 1
	v_cmp_eq_u32_e64 s[2:3], 0, v1
